# critical-path tail trim: CUs that ran a gdn_scan unit / one of the 16 longest dsa units answer their later queue polls with empty instead of the atomic round trip
# baseline (speedup 1.0000x reference)
_Z10fwd_kernel6Params:
	s_mov_b32 s100, 0
	v_writelane_b32 v255, s100, 13
	v_writelane_b32 v255, s100, 14
	s_mov_b32 s100, 0
	v_writelane_b32 v255, s100, 7
	s_mov_b32 s100, 0
	v_writelane_b32 v255, s100, 9
	s_mov_b32 s88, s2
	s_load_dword s2, s[0:1], 0xc0
	v_cmp_gt_u32_e32 vcc, 16, v0
	s_waitcnt lgkmcnt(0)
	v_writelane_b32 v252, s2, 0
	s_add_u32 s2, s0, 0xc0
	s_addc_u32 s3, s1, 0
	v_writelane_b32 v252, s2, 1
	s_nop 1
	v_writelane_b32 v252, s3, 2
	s_and_saveexec_b64 s[2:3], vcc
	v_lshl_add_u32 v1, v0, 2, 0
	v_add_u32_e32 v1, 0x21000, v1
	v_mov_b32_e32 v2, 0
	ds_write_b32 v1, v2
	s_or_b64 exec, exec, s[2:3]
	s_load_dwordx4 s[84:87], s[0:1], 0xa8
	v_cmp_gt_u32_e32 vcc, 21, v0
	s_and_saveexec_b64 s[2:3], vcc
	s_cbranch_execz .LBB0_4
	v_lshlrev_b32_e32 v1, 3, v0
	global_load_dwordx2 v[2:3], v1, s[0:1]
	v_add_u32_e32 v1, 0, v1
	v_add_u32_e32 v1, 0x21040, v1
	s_waitcnt vmcnt(0)
	ds_write_b64 v1, v[2:3]

.LBB0_483:
	s_waitcnt vmcnt(0) lgkmcnt(0)
	s_barrier
	s_and_saveexec_b64 s[6:7], s[36:37]
	s_cbranch_execz .LBB0_485
	v_mov_b64_e32 v[4:5], s[0:1]
	v_readlane_b32 vcc_lo, v255, 13
	v_mov_b32_e32 v1, 0x7fffffff
	s_cmp_eq_u32 vcc_lo, 1
	s_cbranch_scc1 .Lq_skip_scan
	global_atomic_add v1, v[4:5], v228, off sc0
.Lq_skip_scan:
	v_mov_b32_e32 v2, s30
	s_waitcnt vmcnt(0) lgkmcnt(0)
	ds_write_b32 v2, v1
.LBB0_485:
	s_or_b64 exec, exec, s[6:7]
	v_mov_b32_e32 v1, s30
	s_waitcnt lgkmcnt(0)
	s_barrier
	ds_read_b32 v1, v1
	s_mov_b64 s[6:7], -1
	s_waitcnt lgkmcnt(0)
	v_cmp_lt_i32_e32 vcc, 15, v1
	v_readfirstlane_b32 s8, v1
	s_cbranch_vccnz .LBB0_482
	v_readlane_b32 s100, v252, 0
	s_cmp_eq_u32 s100, 0x100
	s_cselect_b32 s100, 1, 0
	v_writelane_b32 v255, s100, 13
	v_mov_b32_e32 v2, v0
	s_lshl_b32 s9, s8, 10
	v_readfirstlane_b32 s6, v2
	s_ashr_i32 s35, s6, 6
	v_readlane_b32 s6, v252, 0
	s_mov_b32 s7, s88
	s_and_b32 s26, s9, 0xfffff000
	s_lshl_b32 s9, s8, 7
	s_ashr_i32 s27, s26, 31
	s_and_b32 s38, s9, 0x180
	s_mov_b64 s[6:7], s[68:69]
	s_lshl_b64 s[10:11], s[26:27], 10
	s_lshl_b32 s9, s38, 1
	s_add_u32 s12, s6, s10
	s_addc_u32 s13, s7, s11
	s_add_u32 s9, s12, s9
	s_addc_u32 s12, s13, 0
	s_add_u32 s20, s9, 0x43a00000
	s_addc_u32 s21, s12, 0
	s_add_u32 s22, s9, 0x44a00000
	s_addc_u32 s23, s12, 0
	s_ashr_i32 s9, s8, 31
	s_lshl_b64 s[12:13], s[8:9], 19
	s_add_u32 s14, s6, s12
	s_addc_u32 s15, s7, s13
	s_add_u32 s18, s14, 0x46a00000
	s_addc_u32 s19, s15, 0
	s_lshl_b64 s[14:15], s[8:9], 20
	s_add_u32 s9, s6, s14
	s_addc_u32 s17, s7, s15
	s_add_u32 s16, s9, 0x45a00000
	s_addc_u32 s17, s17, 0
	s_cmp_lt_i32 s35, 4
	s_cselect_b64 s[24:25], -1, 0
	v_add_u32_e32 v4, 0xffffff00, v2
	v_lshlrev_b32_e32 v5, 4, v2
	v_ashrrev_i32_e32 v150, 4, v2
	v_add_u32_e32 v6, 0x100, v2
	v_add_u32_e32 v7, 0x200, v2
	s_and_b64 vcc, exec, s[24:25]
	v_lshrrev_b32_e32 v1, 3, v2
	v_and_b32_e32 v148, 0xf0, v5
	v_ashrrev_i32_e32 v152, 4, v4
	v_ashrrev_i32_e32 v151, 31, v150
	v_ashrrev_i32_e32 v154, 4, v6
	v_ashrrev_i32_e32 v156, 4, v7
	v_lshlrev_b32_e32 v158, 3, v4
	v_and_b32_e32 v212, 0x70, v5
	v_lshrrev_b32_e32 v211, 3, v4
	v_lshrrev_b32_e32 v210, 3, v6
	v_lshrrev_b32_e32 v201, 3, v7
	s_barrier
	s_cbranch_vccnz .LBB0_488
	v_mov_b32_e32 v149, v3
	v_ashrrev_i32_e32 v153, 31, v152
	v_lshl_add_u64 v[4:5], s[20:21], 0, v[148:149]
	v_lshlrev_b64 v[12:13], 10, v[152:153]
	v_lshl_add_u64 v[6:7], s[22:23], 0, v[148:149]
	v_lshl_add_u64 v[8:9], v[4:5], 0, v[12:13]
	global_load_dwordx4 v[8:11], v[8:9], off
	v_lshl_add_u64 v[12:13], v[6:7], 0, v[12:13]
	v_lshlrev_b64 v[20:21], 10, v[150:151]
	global_load_dwordx4 v[12:15], v[12:13], off
	v_lshl_add_u64 v[16:17], v[4:5], 0, v[20:21]
	v_ashrrev_i32_e32 v155, 31, v154
	global_load_dwordx4 v[16:19], v[16:17], off
	v_lshl_add_u64 v[20:21], v[6:7], 0, v[20:21]
	v_lshlrev_b64 v[28:29], 10, v[154:155]
	v_ashrrev_i32_e32 v157, 31, v156
	global_load_dwordx4 v[20:23], v[20:21], off
	v_lshl_add_u64 v[24:25], v[4:5], 0, v[28:29]
	v_lshlrev_b64 v[36:37], 10, v[156:157]
	global_load_dwordx4 v[24:27], v[24:25], off
	v_lshl_add_u64 v[28:29], v[6:7], 0, v[28:29]
	v_lshl_add_u64 v[4:5], v[4:5], 0, v[36:37]
	global_load_dwordx4 v[28:31], v[28:29], off
	v_ashrrev_i32_e32 v159, 31, v158
	global_load_dwordx4 v[32:35], v[4:5], off
	v_lshl_add_u64 v[4:5], v[6:7], 0, v[36:37]
	global_load_dwordx4 v[36:39], v[4:5], off
	v_lshlrev_b64 v[4:5], 1, v[158:159]
	v_lshl_add_u64 v[6:7], s[18:19], 0, v[4:5]
	v_lshl_add_u64 v[4:5], s[16:17], 0, v[4:5]
	global_load_dwordx4 v[40:43], v[6:7], off
	global_load_dwordx4 v[48:51], v[4:5], off
	v_add_u32_e32 v6, 0x800, v158
	v_ashrrev_i32_e32 v7, 31, v6
	v_lshlrev_b64 v[6:7], 1, v[6:7]
	v_lshl_add_u64 v[44:45], s[18:19], 0, v[6:7]
	v_lshl_add_u64 v[4:5], s[16:17], 0, v[6:7]
	global_load_dwordx4 v[44:47], v[44:45], off
	s_mov_b32 s9, s42
	global_load_dwordx4 v[52:55], v[4:5], off
	v_add_u32_e32 v4, 0x1000, v158
	v_ashrrev_i32_e32 v5, 31, v4
	v_lshl_add_u64 v[4:5], v[4:5], 1, s[16:17]
	global_load_dwordx4 v[56:59], v[4:5], off
	v_add_u32_e32 v4, 0x1800, v158
	v_ashrrev_i32_e32 v5, 31, v4
	v_lshl_add_u64 v[4:5], v[4:5], 1, s[16:17]
	global_load_dwordx4 v[4:7], v[4:5], off
	v_add_u32_e32 v60, s9, v148
	v_mad_u64_u32 v[62:63], s[28:29], v152, s57, v[60:61]
	s_waitcnt vmcnt(0) lgkmcnt(0)
	ds_write2_b64 v62, v[8:9], v[10:11] offset1:1
	v_add_u32_e32 v8, 0x4200, v62
	ds_write2_b64 v8, v[12:13], v[14:15] offset1:1
	v_mad_u64_u32 v[8:9], s[28:29], v150, s57, v[60:61]
	ds_write2_b64 v8, v[16:17], v[18:19] offset1:1
	v_add_u32_e32 v8, 0x4200, v8
	ds_write2_b64 v8, v[20:21], v[22:23] offset1:1
	v_mad_u64_u32 v[8:9], s[28:29], v154, s57, v[60:61]
	ds_write2_b64 v8, v[24:25], v[26:27] offset1:1
	v_add_u32_e32 v8, 0x4200, v8
	ds_write2_b64 v8, v[28:29], v[30:31] offset1:1
	v_mad_u64_u32 v[8:9], s[28:29], v156, s57, v[60:61]
	ds_write2_b64 v8, v[32:33], v[34:35] offset1:1
	v_add_u32_e32 v8, 0x4200, v8
	ds_write2_b64 v8, v[36:37], v[38:39] offset1:1
	v_add_u32_e32 v8, s9, v212
	s_movk_i32 s9, 0x88
	v_mad_u64_u32 v[10:11], s[28:29], v211, s9, v[8:9]
	v_add_u32_e32 v9, 0x8400, v10
	v_mad_u64_u32 v[12:13], s[28:29], v1, s9, v[8:9]
	ds_write2_b64 v9, v[40:41], v[42:43] offset1:1
	v_add_u32_e32 v9, 0x8400, v12
	ds_write2_b64 v9, v[44:45], v[46:47] offset1:1
	v_add_u32_e32 v9, 0xa600, v10
	ds_write2_b64 v9, v[48:49], v[50:51] offset1:1
	v_add_u32_e32 v9, 0xa600, v12
	ds_write2_b64 v9, v[52:53], v[54:55] offset1:1
	v_mul_lo_u32 v9, v210, s9
	v_add3_u32 v9, v8, v9, s58
	ds_write2_b64 v9, v[56:57], v[58:59] offset1:1
	v_mul_lo_u32 v9, v201, s9
	v_add3_u32 v8, v8, v9, s58
	ds_write2_b64 v8, v[4:5], v[6:7] offset1:1

.LBB0_504:
	s_barrier
	s_and_saveexec_b64 s[8:9], s[0:1]
	s_cbranch_execz .LBB0_506
	s_waitcnt vmcnt(0)
	v_mov_b64_e32 v[4:5], s[6:7]
	v_readlane_b32 vcc_lo, v255, 13
	v_mov_b32_e32 v1, 0x7fffffff
	s_cmp_eq_u32 vcc_lo, 1
	s_cbranch_scc1 .Lq_skip_idx
	global_atomic_add v1, v[4:5], v228, off sc0
.Lq_skip_idx:
	v_mov_b32_e32 v2, s12
	s_waitcnt vmcnt(0) lgkmcnt(0)
	ds_write_b32 v2, v1

.LBB0_515:
	s_waitcnt lgkmcnt(0)
	s_barrier
	s_and_saveexec_b64 s[0:1], s[36:37]
	s_cbranch_execz .LBB0_517
	s_waitcnt vmcnt(0)
	v_mov_b64_e32 v[4:5], s[6:7]
	v_readlane_b32 vcc_lo, v255, 13
	v_mov_b32_e32 v1, 0x7fffffff
	s_cmp_eq_u32 vcc_lo, 1
	s_cbranch_scc1 .Lq_skip_fox
	global_atomic_add v1, v[4:5], v228, off sc0
.Lq_skip_fox:
	v_mov_b32_e32 v2, s16
	s_waitcnt vmcnt(0) lgkmcnt(0)
	ds_write_b32 v2, v1

.LBB0_540:
	s_waitcnt lgkmcnt(0)
	s_barrier
	s_and_saveexec_b64 s[6:7], s[0:1]
	s_cbranch_execz .LBB0_542
	s_waitcnt vmcnt(0)
	v_mov_b64_e32 v[4:5], s[4:5]
	v_readlane_b32 vcc_lo, v255, 13
	v_mov_b32_e32 v1, 0x7fffffff
	s_cmp_eq_u32 vcc_lo, 1
	s_cbranch_scc1 .Lq_skip_rets
	global_atomic_add v1, v[4:5], v228, off sc0
.Lq_skip_rets:
	v_mov_b32_e32 v2, s8
	s_waitcnt vmcnt(0) lgkmcnt(0)
	ds_write_b32 v2, v1

.LBB0_546:
	s_mov_b32 s100, 0
	v_writelane_b32 v255, s100, 13
	v_readlane_b32 s0, v253, 26
	s_add_i32 s18, s0, 5
	s_cmp_lt_i32 s18, s91
	s_cselect_b64 s[0:1], -1, 0
	s_and_b64 s[2:3], s[2:3], s[0:1]
	s_andn2_b64 vcc, exec, s[2:3]
	s_cbranch_vccnz .LBB0_600
	s_waitcnt vmcnt(0)
	s_waitcnt vmcnt(0) lgkmcnt(0)
	s_barrier
	s_mov_b64 s[2:3], exec
	v_readlane_b32 s4, v252, 3
	v_readlane_b32 s5, v252, 4
	s_and_b64 s[4:5], s[2:3], s[4:5]
	s_mov_b64 exec, s[4:5]
	s_cbranch_execz .LBB0_599
	v_readlane_b32 s4, v253, 15
	s_waitcnt vmcnt(0) expcnt(0) lgkmcnt(0)
	s_nop 0
	v_mov_b32_e32 v1, s4
	ds_read_b32 v4, v1
	v_readlane_b32 s4, v253, 16
	s_waitcnt lgkmcnt(0)
	v_cmp_ne_u32_e32 vcc, 0, v4
	v_mov_b32_e32 v1, s4
	ds_read_b32 v2, v1
	s_cbranch_vccnz .LBB0_563
	v_readlane_b32 s6, v252, 1
	v_readlane_b32 s7, v252, 2
	s_load_dwordx2 s[4:5], s[6:7], 0x4
	v_readlane_b32 s6, v252, 0
	s_mov_b32 s11, 1
	s_waitcnt lgkmcnt(0)
	s_mul_i32 s10, s4, s6
	s_mul_i32 s10, s10, s5
	s_branch .LBB0_551

.LBB0_1136:
	s_waitcnt vmcnt(0) lgkmcnt(0)
	s_barrier
	s_and_saveexec_b64 s[2:3], s[36:37]
	s_cbranch_execz .LBB0_1138
	v_mov_b64_e32 v[4:5], s[0:1]
	v_readlane_b32 vcc_lo, v255, 14
	v_mov_b32_e32 v1, 0x7fffffff
	s_cmp_eq_u32 vcc_lo, 1
	s_cbranch_scc1 .Lq_skip_aret
	global_atomic_add v1, v[4:5], v228, off sc0
.Lq_skip_aret:
	v_mov_b32_e32 v2, s10
	s_waitcnt vmcnt(0) lgkmcnt(0)
	ds_write_b32 v2, v1

.LBB0_1211:
	s_waitcnt vmcnt(0) lgkmcnt(0)
	s_barrier
	s_and_saveexec_b64 s[0:1], s[36:37]
	s_cbranch_execz .LBB0_1213
	v_mov_b64_e32 v[4:5], s[6:7]
	v_readlane_b32 vcc_lo, v255, 14
	v_mov_b32_e32 v1, 0x7fffffff
	s_cmp_eq_u32 vcc_lo, 1
	s_cbranch_scc1 .Lq_skip_dsa
	global_atomic_add v1, v[4:5], v228, off sc0

.LBB0_1213:
	s_or_b64 exec, exec, s[0:1]
	v_mov_b32_e32 v1, s16
	s_waitcnt lgkmcnt(0)
	s_barrier
	ds_read_b32 v1, v1
	s_mov_b64 s[0:1], -1
	s_waitcnt lgkmcnt(0)
	v_cmp_lt_i32_e32 vcc, s75, v1
	v_readfirstlane_b32 s8, v1
	s_cbranch_vccnz .LBB0_1210
	v_readlane_b32 s100, v252, 0
	s_cmp_eq_u32 s100, 0x100
	s_cselect_b32 s100, 16, 0
	s_cmp_lt_u32 s8, s100
	s_cselect_b32 s100, 1, 0
	v_writelane_b32 v255, s100, 14
	v_mov_b32_e32 v4, v0
	v_readlane_b32 s0, v252, 0
	s_mov_b32 s1, s88
	s_lshl_b32 s20, s8, 4
	v_readfirstlane_b32 s21, v4
	s_lshr_b32 s0, s21, 1
	s_andn2_b32 s20, s20, 63
	s_and_b32 s0, s0, 32
	s_and_b32 s10, s21, 0xffffff80
	s_sub_i32 s14, s0, s20
	s_ashr_i32 s11, s10, 31
	s_and_b32 s18, s8, 3
	s_mov_b64 s[8:9], s[68:69]
	s_add_i32 s15, s14, 0xfc0
	s_lshl_b64 s[0:1], s[10:11], 1
	s_add_u32 s0, s8, s0
	s_addc_u32 s1, s9, s1
	v_and_b32_e32 v8, 31, v4
	s_add_u32 s0, s0, 0x2de00000
	v_or_b32_e32 v1, s15, v8
	s_addc_u32 s1, s1, 0
	s_lshl_b32 s19, s18, 12
	v_bfe_u32 v9, v4, 5, 1
	v_add_u32_e32 v2, s19, v1
	v_mov_b64_e32 v[6:7], s[0:1]
	s_movk_i32 s0, 0xc00
	v_mad_u64_u32 v[6:7], s[0:1], v2, s0, v[6:7]
	v_lshlrev_b32_e32 v148, 4, v9
	v_mov_b32_e32 v149, v3
	v_lshl_add_u64 v[6:7], v[6:7], 0, v[148:149]
	global_load_dwordx4 v[100:103], v[6:7], off
	global_load_dwordx4 v[104:107], v[6:7], off offset:32
	global_load_dwordx4 v[108:111], v[6:7], off offset:64
	global_load_dwordx4 v[112:115], v[6:7], off offset:96
	global_load_dwordx4 v[116:119], v[6:7], off offset:128
	global_load_dwordx4 v[120:123], v[6:7], off offset:160
	global_load_dwordx4 v[124:127], v[6:7], off offset:192
	global_load_dwordx4 v[128:131], v[6:7], off offset:224
	v_lshl_add_u64 v[6:7], v[2:3], 2, s[8:9]
	v_add_co_u32_e32 v6, vcc, 0x49240000, v6
	s_movk_i32 s0, 0x204
	s_nop 0
	v_addc_co_u32_e32 v7, vcc, 0, v7, vcc
	global_load_dword v10, v[6:7], off
	v_cmp_gt_i32_e32 vcc, s0, v4
	s_waitcnt lgkmcnt(0)
	s_barrier
	s_and_saveexec_b64 s[0:1], vcc
	s_cbranch_execz .LBB0_1217
	v_ashrrev_i32_e32 v5, 31, v4
	v_lshl_add_u64 v[6:7], v[4:5], 2, s[8:9]
	s_mov_b64 s[12:13], 0x300000
	v_add_u32_e32 v1, 0xfffffe00, v4
	v_lshl_add_u32 v11, v4, 2, s17
	v_lshl_add_u64 v[6:7], v[6:7], 0, s[12:13]
	s_mov_b64 s[12:13], 0

.LBB0_1328:
	s_waitcnt lgkmcnt(0)
	s_barrier
	s_and_saveexec_b64 s[0:1], s[36:37]
	s_cbranch_execz .LBB0_1330
	v_mov_b64_e32 v[4:5], s[4:5]
	v_readlane_b32 vcc_lo, v255, 14
	v_mov_b32_e32 v1, 0x7fffffff
	s_cmp_eq_u32 vcc_lo, 1
	s_cbranch_scc1 .Lq_skip_cvte
	global_atomic_add v1, v[4:5], v228, off sc0
.Lq_skip_cvte:
	v_mov_b32_e32 v2, s33
	s_waitcnt vmcnt(0) lgkmcnt(0)
	ds_write_b32 v2, v1

.LBB0_1390:
	s_mov_b32 s100, 0
	v_writelane_b32 v255, s100, 14
	v_readlane_b32 s0, v253, 26
	s_add_i32 s18, s0, 7
	s_cmp_lt_i32 s18, s91
	s_cselect_b64 s[0:1], -1, 0
	s_and_b64 s[2:3], s[2:3], s[0:1]
	s_andn2_b64 vcc, exec, s[2:3]
	s_cbranch_vccnz .LBB0_1444
	s_waitcnt vmcnt(0)
	s_waitcnt vmcnt(0) lgkmcnt(0)
	s_barrier
	s_mov_b64 s[2:3], exec
	v_readlane_b32 s4, v252, 3
	v_readlane_b32 s5, v252, 4
	s_and_b64 s[4:5], s[2:3], s[4:5]
	s_mov_b64 exec, s[4:5]
	s_cbranch_execz .LBB0_1443
	v_readlane_b32 s4, v253, 15
	s_waitcnt vmcnt(0) expcnt(0) lgkmcnt(0)
	s_nop 0
	v_mov_b32_e32 v1, s4
	ds_read_b32 v4, v1
	v_readlane_b32 s4, v253, 16
	s_waitcnt lgkmcnt(0)
	v_cmp_ne_u32_e32 vcc, 0, v4
	v_mov_b32_e32 v1, s4
	ds_read_b32 v2, v1
	s_cbranch_vccnz .LBB0_1407
	v_readlane_b32 s6, v252, 1
	v_readlane_b32 s7, v252, 2
	s_load_dwordx2 s[4:5], s[6:7], 0x4
	v_readlane_b32 s6, v252, 0
	s_mov_b32 s11, 1
	s_waitcnt lgkmcnt(0)
	s_mul_i32 s10, s4, s6
	s_mul_i32 s10, s10, s5
	s_branch .LBB0_1395
